# v18 plus layer-loop grid barrier waiters polling the top-level generation word directly
# speedup vs baseline: 1.0036x; 1.0036x over previous
; __device__ __forceinline__ unsigned xb_ld(unsigned* p)              { return __hip_atomic_load(p, __ATOMIC_RELAXED, __HIP_MEMORY_SCOPE_AGENT); }
; __device__ __forceinline__ unsigned xb_add(unsigned* p, unsigned v) { return __hip_atomic_fetch_add(p, v, __ATOMIC_RELAXED, __HIP_MEMORY_SCOPE_AGENT); }
; #define XB_SPIN(cond, bar) do { unsigned _sp = 0; while (cond) { __builtin_amdgcn_s_sleep(1); \
;     if ((++_sp & 255u) == 0u) { if (xb_ld(&(bar)[XB_TMO])) break; if (_sp > XB_SPIN_CAP) { atomicAdd(&(bar)[XB_TMO], 1u); break; } } } } while (0)
; __device__ __forceinline__ void xcd_barrier(const XcdBarrier& b, int tid_) {
;     asm volatile("s_waitcnt vmcnt(0)" ::: "memory");
;     __syncthreads();
;     if (tid_ == 0) {
;         unsigned* bar = b.bar;
;         __builtin_amdgcn_s_waitcnt(0);
;         unsigned nloc = b.st[0], nx = b.st[1];
;         if (nloc == 0u) { unsigned bal_; xcd_barrier_complete(bar, b.x, nloc, nx, bal_); b.st[0] = nloc; b.st[1] = nx;
;             b.st[3] = (bal_ ? b.st[2] * 8u + b.x : (unsigned)blockIdx.x) + 1u; }
;         const unsigned old = xb_add(&bar[XB_XSUB(b.x)], 1u);
;         const unsigned gen = old / nloc;
;         if (old + 1u == (gen + 1u) * nloc) {
;             __builtin_amdgcn_fence(__ATOMIC_RELEASE, "agent");
;             asm volatile("s_waitcnt vmcnt(0)" ::: "memory");
;             const unsigned og = xb_add(&bar[XB_TOP], 1u);
;             const unsigned tg = og / nx;
;             if (og + 1u == (tg + 1u) * nx) xb_add(&bar[XB_TOPGEN], 1u);
;             else XB_SPIN(xb_ld(&bar[XB_TOPGEN]) == tg, bar);
;             __builtin_amdgcn_fence(__ATOMIC_ACQUIRE, "agent");
;             xb_add(&bar[XB_XGEN(b.x)], 1u);
;             asm volatile("s_waitcnt vmcnt(0)" ::: "memory");
.LBB0_386:
	s_add_u32 s42, s72, 0x4200
	s_addc_u32 s43, s73, 0
	s_lshl_b32 s0, s33, 8
	s_add_u32 s0, s66, s0
	s_addc_u32 s1, s67, 0
	s_add_u32 s2, s0, 0x1400
	s_addc_u32 s3, s1, 0
	s_add_u32 s74, s72, 0x7500
	s_addc_u32 s75, s73, 0
	v_writelane_b32 v255, s2, 18
	s_add_u32 s0, s72, 0x7400
	s_addc_u32 s1, s73, 0
	v_writelane_b32 v255, s3, 19
	v_writelane_b32 v255, s0, 20
	s_mov_b32 s23, 0
	s_mov_b32 s59, 2
	v_writelane_b32 v255, s1, 21
	s_add_u32 s0, s72, 0x7500
	s_addc_u32 s1, s73, 0
	v_writelane_b32 v255, s0, 9
	s_add_u32 s50, s72, 0x4400
	s_addc_u32 s51, s73, 0
	v_writelane_b32 v255, s1, 10
	s_mov_b64 s[0:1], 0
	v_writelane_b32 v255, s0, 6
	s_mov_b32 s95, 0x10000
	v_mov_b32_e32 v128, 0
	v_writelane_b32 v255, s1, 7
	s_add_i32 s0, 0, 0x20160
	v_writelane_b32 v255, s0, 15
	s_add_i32 s0, 0, 0x20164
	v_writelane_b32 v255, s0, 22
	s_add_i32 s0, 0, 0x20168
	v_writelane_b32 v255, s0, 23
	v_writelane_b32 v255, s42, 11
	s_mov_b64 s[38:39], 0x20000
	s_mov_b64 s[40:41], 0x80
	v_writelane_b32 v255, s43, 12
	v_writelane_b32 v255, s74, 16
	s_movk_i32 s90, 0x100
	s_mov_b64 s[44:45], 0x100
	v_writelane_b32 v255, s75, 17
	v_writelane_b32 v255, s50, 13
	s_movk_i32 s96, 0x500
	v_mov_b32_e32 v248, 1
	v_writelane_b32 v255, s51, 14
	s_mov_b32 s53, 0xffff0000
	v_mov_b32_e32 v249, 0x3727c5ac
	s_mov_b32 s52, 0xf800000
	v_mov_b32_e32 v250, 0x260
	s_movk_i32 s55, 0x7fff
	s_brev_b32 s47, 1
	s_mov_b32 s54, 0xc2fe0000
	s_mov_b32 s65, 0x40c0c00
	s_mov_b32 s48, 0xc0e00000
	v_mbcnt_hi_u32_b32 v251, -1, v142
	v_mov_b32_e32 v240, 0x3836d887
	v_mov_b32_e32 v241, 0x36b6d887
	v_mov_b32_e32 v242, 0x500
	v_mov_b32_e32 v212, 0xff800000
	v_mov_b64_e32 v[244:245], 0x100
	v_mov_b64_e32 v[218:219], 0xff
	v_mov_b32_e32 v213, 0x42fe0000
	v_mov_b32_e32 v214, 0x40e00000
	s_mov_b32 s64, 0x38388159
	s_mov_b32 s62, s23
	v_writelane_b32 v255, s97, 24
	s_branch .LBB0_390

; __device__ __forceinline__ unsigned xb_add(unsigned* p, unsigned v) { return __hip_atomic_fetch_add(p, v, __ATOMIC_RELAXED, __HIP_MEMORY_SCOPE_AGENT); }
; __device__ __forceinline__ void xcd_barrier(const XcdBarrier& b, int tid_) {
;     ...
;             __builtin_amdgcn_fence(__ATOMIC_ACQUIRE, "agent");
;             xb_add(&bar[XB_XGEN(b.x)], 1u);
.LBB0_533:
	s_or_b64 exec, exec, s[2:3]
	s_mov_b64 s[2:3], exec
	v_mbcnt_lo_u32_b32 v0, s2, 0
	v_mbcnt_hi_u32_b32 v0, s3, v0
	v_cmp_eq_u32_e32 vcc, 0, v0
	s_waitcnt vmcnt(0)
	buffer_inv sc1
	s_and_saveexec_b64 s[4:5], vcc
	s_cbranch_execz .LBB0_535
	s_bcnt1_i32_b64 s2, s[2:3]
	v_mov_b32_e32 v0, s2
	global_atomic_add v128, v0, s[74:75] offset:64

; __device__ __forceinline__ unsigned xb_add(unsigned* p, unsigned v) { return __hip_atomic_fetch_add(p, v, __ATOMIC_RELAXED, __HIP_MEMORY_SCOPE_AGENT); }
; __device__ __forceinline__ void xcd_barrier(const XcdBarrier& b, int tid_) {
;     ...
;             xb_add(&bar[XB_XGEN(b.x)], 1u);
.LBB0_3631:
	s_bcnt1_i32_b64 s2, s[2:3]
	v_mov_b32_e32 v0, s2
	global_atomic_add v128, v0, s[74:75] offset:64
	s_getpc_b64 s[98:99]
